# P7 final output stores with sc1 (write-through)
# speedup vs baseline: 1.0036x; 1.0036x over previous
.LBB0_718:
	s_ashr_i32 s7, s6, 31
	s_lshl_b64 s[0:1], s[6:7], 2
	s_add_u32 s0, s16, s0
	s_addc_u32 s1, s17, s1
	global_load_dwordx2 v[28:29], v[20:21], off offset:-1024 nt
	global_load_dwordx2 v[26:27], v[20:21], off offset:-512 nt
	global_load_dwordx2 v[24:25], v[20:21], off nt
	global_load_dwordx2 v[30:31], v[20:21], off offset:-1536 nt
	global_load_dwordx4 v[36:39], v17, s[0:1]
	v_lshl_add_u64 v[20:21], v[20:21], 0, s[10:11]
	s_waitcnt vmcnt(4)
	v_lshlrev_b32_e32 v32, 16, v28
	s_waitcnt vmcnt(3)
	v_lshlrev_b32_e32 v35, 16, v27
	v_and_b32_e32 v46, 0xffff0000, v27
	v_lshlrev_b32_e32 v42, 16, v26
	s_waitcnt vmcnt(0)
	v_readfirstlane_b32 s1, v36
	s_ashr_i32 s18, s1, 16
	v_readfirstlane_b32 s20, v37
	s_and_b32 s22, s1, 0xffff
	s_ashr_i32 s19, s18, 31
	s_lshl_b32 s1, s18, 2
	s_ashr_i32 s0, s20, 16
	s_add_i32 s1, s3, s1
	s_lshl_b64 s[18:19], s[18:19], 18
	s_add_u32 s18, s2, s18
	v_and_b32_e32 v43, 0xffff0000, v26
	v_lshlrev_b32_e32 v26, 16, v24
	v_and_b32_e32 v27, 0xffff0000, v24
	v_mov_b32_e32 v24, s1
	s_addc_u32 s19, s13, s19
	s_lshl_b32 s23, s0, 2
	v_lshlrev_b32_e32 v48, 16, v25
	v_and_b32_e32 v124, 0xffff0000, v25
	ds_read_b32 v25, v24
	s_ashr_i32 s1, s0, 31
	s_and_b32 s24, s20, 0xffff
	s_add_i32 s20, s3, s23
	s_lshl_b32 s21, s22, 2
	s_lshl_b64 s[0:1], s[0:1], 18
	v_mov_b32_e32 v36, s20
	v_readfirstlane_b32 s7, v38
	s_add_u32 s0, s2, s0
	ds_read_b32 v38, v36
	v_mov_b32_e32 v24, s21
	global_load_dword v24, v24, s[18:19]
	s_addc_u32 s1, s13, s1
	s_lshl_b32 s19, s24, 2
	s_ashr_i32 s20, s7, 16
	v_readfirstlane_b32 s15, v39
	v_mov_b32_e32 v37, s19
	s_ashr_i32 s21, s20, 31
	s_lshl_b32 s19, s20, 2
	s_ashr_i32 s18, s15, 16
	s_and_b32 s7, s7, 0xffff
	s_waitcnt lgkmcnt(1)
	v_add_u32_e32 v36, s22, v25
	global_load_dword v25, v37, s[0:1]
	s_add_i32 s19, s3, s19
	s_lshl_b64 s[0:1], s[20:21], 18
	s_add_u32 s0, s2, s0
	v_mov_b32_e32 v39, s19
	s_addc_u32 s1, s13, s1
	s_lshl_b32 s20, s7, 2
	s_lshl_b32 s21, s18, 2
	ds_read_b32 v47, v39
	v_mov_b32_e32 v39, s20
	s_add_i32 s20, s3, s21
	s_ashr_i32 s19, s18, 31
	v_mov_b32_e32 v45, s20
	v_ashrrev_i32_e32 v37, 31, v36
	s_and_b32 s15, s15, 0xffff
	s_waitcnt lgkmcnt(1)
	v_add_u32_e32 v38, s24, v38
	s_lshl_b64 s[18:19], s[18:19], 18
	ds_read_b32 v49, v45
	v_lshlrev_b64 v[36:37], 10, v[36:37]
	global_load_dword v44, v39, s[0:1]
	s_add_u32 s0, s2, s18
	v_ashrrev_i32_e32 v39, 31, v38
	v_lshl_add_u64 v[36:37], v[18:19], 0, v[36:37]
	s_addc_u32 s1, s13, s19
	s_lshl_b32 s18, s15, 2
	v_lshlrev_b64 v[38:39], 10, v[38:39]
	v_mov_b32_e32 v50, s18
	v_lshl_add_u64 v[38:39], v[18:19], 0, v[38:39]
	global_load_dword v53, v[36:37], off nt
	global_load_dword v55, v[36:37], off offset:256 nt
	global_load_dword v56, v[36:37], off offset:512 nt
	global_load_dword v59, v[36:37], off offset:768 nt
	global_load_dword v61, v[38:39], off nt
	global_load_dword v63, v[38:39], off offset:256 nt
	global_load_dword v66, v[38:39], off offset:512 nt
	global_load_dword v76, v[38:39], off offset:768 nt
	global_load_dword v45, v50, s[0:1]
	s_waitcnt lgkmcnt(1)
	v_add_u32_e32 v36, s7, v47
	v_ashrrev_i32_e32 v37, 31, v36
	v_lshlrev_b64 v[36:37], 10, v[36:37]
	s_waitcnt lgkmcnt(0)
	v_add_u32_e32 v38, s15, v49
	v_lshl_add_u64 v[36:37], v[18:19], 0, v[36:37]
	v_ashrrev_i32_e32 v39, 31, v38
	global_load_dword v82, v[36:37], off nt
	global_load_dword v84, v[36:37], off offset:256 nt
	global_load_dword v86, v[36:37], off offset:512 nt
	global_load_dword v88, v[36:37], off offset:768 nt
	v_lshlrev_b64 v[36:37], 10, v[38:39]
	v_lshl_add_u64 v[36:37], v[18:19], 0, v[36:37]
	global_load_dword v38, v[36:37], off nt
	global_load_dword v90, v[36:37], off offset:256 nt
	global_load_dword v92, v[36:37], off offset:512 nt
	global_load_dword v94, v[36:37], off offset:768 nt
	v_lshlrev_b32_e32 v40, 16, v30
	v_and_b32_e32 v41, 0xffff0000, v30
	v_and_b32_e32 v33, 0xffff0000, v28
	v_lshlrev_b32_e32 v30, 16, v31
	v_and_b32_e32 v31, 0xffff0000, v31
	v_lshlrev_b32_e32 v28, 16, v29
	v_and_b32_e32 v29, 0xffff0000, v29
	s_add_i32 s4, s4, s80
	s_add_i32 s6, s6, s14
	s_cmp_gt_i32 s4, 0xffff
	s_waitcnt vmcnt(18)
	v_pk_mul_f32 v[24:25], v[24:25], s[12:13] op_sel_hi:[1,0]
	s_nop 0
	v_mov_b32_e32 v37, v24
	v_mov_b32_e32 v47, v24
	v_mov_b32_e32 v49, v24
	v_mov_b32_e32 v39, v25
	s_waitcnt vmcnt(16)
	v_cvt_f32_fp8_e32 v50, v53
	s_waitcnt vmcnt(15)
	v_cvt_f32_fp8_sdwa v58, v55 src0_sel:BYTE_2
	v_cvt_f32_fp8_sdwa v60, v55 src0_sel:BYTE_3
	s_waitcnt vmcnt(13)
	v_cvt_f32_fp8_e32 v70, v59
	v_cvt_f32_fp8_sdwa v72, v59 src0_sel:BYTE_1
	v_cvt_f32_fp8_sdwa v74, v59 src0_sel:BYTE_2
	v_cvt_f32_fp8_sdwa v77, v59 src0_sel:BYTE_3
	s_waitcnt vmcnt(12)
	v_cvt_f32_fp8_e32 v78, v61
	v_cvt_f32_fp8_sdwa v79, v61 src0_sel:BYTE_1
	v_cvt_f32_fp8_sdwa v80, v61 src0_sel:BYTE_2
	v_cvt_f32_fp8_sdwa v81, v61 src0_sel:BYTE_3
	s_waitcnt vmcnt(11)
	v_cvt_f32_fp8_sdwa v59, v63 src0_sel:BYTE_2
	v_cvt_f32_fp8_sdwa v61, v63 src0_sel:BYTE_3
	v_cvt_f32_fp8_sdwa v51, v53 src0_sel:BYTE_1
	v_cvt_f32_fp8_e32 v54, v55
	v_cvt_f32_fp8_sdwa v57, v55 src0_sel:BYTE_1
	v_cvt_f32_fp8_e32 v62, v56
	v_cvt_f32_fp8_sdwa v64, v56 src0_sel:BYTE_1
	v_cvt_f32_fp8_e32 v55, v63
	v_cvt_f32_fp8_sdwa v83, v63 src0_sel:BYTE_1
	s_waitcnt vmcnt(10)
	v_cvt_f32_fp8_e32 v63, v66
	v_cvt_f32_fp8_sdwa v65, v66 src0_sel:BYTE_1
	v_cvt_f32_fp8_sdwa v52, v53 src0_sel:BYTE_2
	v_cvt_f32_fp8_sdwa v53, v53 src0_sel:BYTE_3
	v_cvt_f32_fp8_sdwa v68, v56 src0_sel:BYTE_3
	v_cvt_f32_fp8_sdwa v69, v66 src0_sel:BYTE_3
	s_waitcnt vmcnt(9)
	v_cvt_f32_fp8_sdwa v75, v76 src0_sel:BYTE_2
	v_pk_mul_f32 v[58:59], v[24:25], v[58:59]
	v_pk_mul_f32 v[60:61], v[24:25], v[60:61]
	v_pk_mul_f32 v[64:65], v[24:25], v[64:65]
	v_pk_mul_f32 v[62:63], v[24:25], v[62:63]
	s_waitcnt vmcnt(7)
	v_cvt_f32_fp8_e32 v96, v82
	v_cvt_f32_fp8_sdwa v97, v82 src0_sel:BYTE_1
	v_pk_fma_f32 v[40:41], v[24:25], v[50:51], v[40:41] op_sel_hi:[0,1,1]
	v_mov_b32_e32 v50, v58
	v_mov_b32_e32 v51, v60
	v_cvt_f32_fp8_e32 v71, v76
	v_cvt_f32_fp8_sdwa v73, v76 src0_sel:BYTE_1
	v_cvt_f32_fp8_sdwa v98, v82 src0_sel:BYTE_2
	v_cvt_f32_fp8_sdwa v99, v82 src0_sel:BYTE_3
	s_waitcnt vmcnt(5)
	v_cvt_f32_fp8_sdwa v114, v86 src0_sel:BYTE_3
	s_waitcnt vmcnt(4)
	v_cvt_f32_fp8_sdwa v120, v88 src0_sel:BYTE_2
	v_pk_fma_f32 v[30:31], v[24:25], v[52:53], v[30:31] op_sel_hi:[0,1,1]
	v_mov_b32_e32 v52, v62
	v_mov_b32_e32 v53, v64
	v_pk_add_f32 v[28:29], v[50:51], v[28:29]
	s_waitcnt vmcnt(3)
	v_cvt_f32_fp8_e32 v50, v38
	v_cvt_f32_fp8_sdwa v51, v38 src0_sel:BYTE_1
	s_waitcnt vmcnt(1)
	v_cvt_f32_fp8_sdwa v115, v92 src0_sel:BYTE_3
	s_waitcnt vmcnt(0)
	v_cvt_f32_fp8_sdwa v121, v94 src0_sel:BYTE_2
	v_cvt_f32_fp8_e32 v100, v84
	v_pk_add_f32 v[42:43], v[52:53], v[42:43]
	v_cvt_f32_fp8_sdwa v52, v38 src0_sel:BYTE_2
	v_cvt_f32_fp8_sdwa v53, v38 src0_sel:BYTE_3
	v_cvt_f32_fp8_e32 v101, v90
	v_pk_mul_f32 v[44:45], v[44:45], s[12:13] op_sel_hi:[1,0]
	v_pk_mul_f32 v[54:55], v[24:25], v[54:55]
	v_pk_mul_f32 v[68:69], v[24:25], v[68:69]
	v_pk_mul_f32 v[74:75], v[24:25], v[74:75]
	v_pk_fma_f32 v[40:41], v[24:25], v[78:79], v[40:41] op_sel:[1,0,0]
	v_add_f32_e32 v32, v54, v32
	v_add_f32_e32 v36, v68, v46
	v_add_f32_e32 v46, v74, v48
	v_pk_fma_f32 v[30:31], v[24:25], v[80:81], v[30:31] op_sel:[1,0,0]
	v_pk_fma_f32 v[40:41], v[44:45], v[96:97], v[40:41] op_sel_hi:[0,1,1]
	v_pk_mul_f32 v[70:71], v[24:25], v[70:71]
	v_pk_mul_f32 v[72:73], v[24:25], v[72:73]
	v_cvt_f32_fp8_sdwa v103, v84 src0_sel:BYTE_1
	v_cvt_f32_fp8_sdwa v104, v84 src0_sel:BYTE_2
	v_cvt_f32_fp8_sdwa v106, v84 src0_sel:BYTE_3
	v_mov_b32_e32 v64, v63
	v_add_f32_e32 v24, v32, v55
	v_add_f32_e32 v32, v36, v69
	v_add_f32_e32 v36, v46, v75
	v_cvt_f32_fp8_sdwa v105, v90 src0_sel:BYTE_2
	v_cvt_f32_fp8_sdwa v107, v90 src0_sel:BYTE_3
	v_pk_fma_f32 v[30:31], v[44:45], v[98:99], v[30:31] op_sel_hi:[0,1,1]
	v_pk_mul_f32 v[74:75], v[44:45], v[114:115]
	v_pk_mul_f32 v[96:97], v[44:45], v[120:121]
	v_pk_fma_f32 v[40:41], v[44:45], v[50:51], v[40:41] op_sel:[1,0,0]
	v_cvt_f32_fp8_sdwa v67, v56 src0_sel:BYTE_2
	v_cvt_f32_fp8_sdwa v55, v90 src0_sel:BYTE_1
	v_pk_add_f32 v[42:43], v[42:43], v[64:65]
	v_pk_mul_f32 v[64:65], v[44:45], v[100:101]
	v_pk_fma_f32 v[30:31], v[44:45], v[52:53], v[30:31] op_sel:[1,0,0]
	v_add_f32_e32 v46, v32, v74
	v_add_f32_e32 v48, v36, v96
	v_mov_b32_e32 v36, v40
	v_mov_b32_e32 v56, v40
	v_mul_f32_e32 v32, v41, v41
	v_cvt_f32_fp8_e32 v108, v86
	v_cvt_f32_fp8_sdwa v110, v86 src0_sel:BYTE_1
	v_cvt_f32_fp8_e32 v109, v92
	v_cvt_f32_fp8_sdwa v111, v92 src0_sel:BYTE_1
	v_add_f32_e32 v24, v24, v64
	v_mov_b32_e32 v38, v30
	v_mov_b32_e32 v82, v30
	v_pk_fma_f32 v[32:33], v[36:37], v[56:57], v[32:33]
	v_cvt_f32_fp8_e32 v116, v88
	v_cvt_f32_fp8_sdwa v118, v88 src0_sel:BYTE_1
	v_cvt_f32_fp8_sdwa v123, v88 src0_sel:BYTE_3
	v_pk_mov_b32 v[50:51], v[30:31], v[44:45] op_sel:[1,0]
	v_mov_b32_e32 v102, v31
	v_add_f32_e32 v88, v24, v65
	v_pk_fma_f32 v[32:33], v[38:39], v[82:83], v[32:33]
	v_mov_b32_e32 v89, v45
	v_mov_b32_e32 v60, v59
	v_mov_b32_e32 v58, v70
	v_mov_b32_e32 v59, v72
	v_mov_b32_e32 v72, v71
	v_pk_mul_f32 v[68:69], v[44:45], v[104:105]
	v_pk_mul_f32 v[70:71], v[44:45], v[106:107]
	v_mov_b32_e32 v54, v88
	v_pk_fma_f32 v[32:33], v[50:51], v[102:103], v[32:33]
	v_pk_add_f32 v[26:27], v[58:59], v[26:27]
	v_cvt_f32_fp8_e32 v117, v94
	v_cvt_f32_fp8_sdwa v119, v94 src0_sel:BYTE_1
	v_pk_add_f32 v[28:29], v[28:29], v[60:61]
	v_mov_b32_e32 v52, v68
	v_mov_b32_e32 v53, v70
	v_add_f32_e32 v46, v46, v75
	v_pk_fma_f32 v[32:33], v[88:89], v[54:55], v[32:33]
	v_cvt_f32_fp8_sdwa v85, v66 src0_sel:BYTE_2
	v_pk_add_f32 v[26:27], v[26:27], v[72:73]
	v_pk_mul_f32 v[60:61], v[44:45], v[110:111]
	v_pk_mul_f32 v[72:73], v[44:45], v[108:109]
	v_mov_b32_e32 v70, v69
	v_pk_add_f32 v[28:29], v[28:29], v[52:53]
	v_mov_b32_e32 v39, v46
	v_mul_f32_e32 v38, v33, v33
	v_cvt_f32_fp8_sdwa v113, v86 src0_sel:BYTE_2
	v_mov_b32_e32 v68, v72
	v_mov_b32_e32 v69, v60
	v_pk_add_f32 v[28:29], v[28:29], v[70:71]
	v_mov_b32_e32 v89, v33
	v_pk_add_f32 v[32:33], v[32:33], v[38:39] op_sel_hi:[1,0]
	v_cvt_f32_fp8_sdwa v59, v92 src0_sel:BYTE_2
	v_mov_b32_e32 v60, v73
	v_add_f32_e32 v90, v48, v97
	v_pk_add_f32 v[36:37], v[42:43], v[68:69]
	v_mov_b32_e32 v48, v28
	v_mov_b32_e32 v66, v28
	v_mov_b32_e32 v33, v35
	v_pk_mul_f32 v[78:79], v[44:45], v[116:117]
	v_pk_mul_f32 v[80:81], v[44:45], v[118:119]
	v_pk_add_f32 v[36:37], v[36:37], v[60:61]
	v_mov_b32_e32 v24, v29
	v_mov_b32_e32 v84, v29
	v_pk_fma_f32 v[32:33], v[48:49], v[66:67], v[32:33]
	v_mov_b32_e32 v93, v44
	v_mov_b32_e32 v72, v78
	v_mov_b32_e32 v73, v80
	v_mov_b32_e32 v92, v36
	v_mov_b32_e32 v112, v36
	v_pk_fma_f32 v[32:33], v[24:25], v[84:85], v[32:33]
	v_mov_b32_e32 v95, v45
	v_cvt_f32_fp8_sdwa v63, v94 src0_sel:BYTE_3
	v_mov_b32_e32 v80, v79
	v_pk_add_f32 v[26:27], v[26:27], v[72:73]
	v_mov_b32_e32 v94, v37
	v_mov_b32_e32 v58, v37
	v_pk_fma_f32 v[32:33], v[92:93], v[112:113], v[32:33]
	v_pk_add_f32 v[26:27], v[26:27], v[80:81]
	v_pk_fma_f32 v[32:33], v[94:95], v[58:59], v[32:33]
	v_cvt_f32_fp8_sdwa v87, v76 src0_sel:BYTE_3
	v_pk_mov_b32 v[42:43], v[26:27], v[44:45] op_sel:[1,0]
	v_mul_f32_e32 v44, v33, v33
	v_mov_b32_e32 v38, v33
	v_pk_add_f32 v[32:33], v[32:33], v[44:45] op_sel_hi:[1,0]
	v_mov_b32_e32 v76, v46
	v_mov_b32_e32 v33, v124
	v_mov_b32_e32 v86, v26
	v_mov_b32_e32 v24, v26
	v_pk_fma_f32 v[32:33], v[46:47], v[76:77], v[32:33]
	v_mov_b32_e32 v122, v42
	v_pk_fma_f32 v[24:25], v[24:25], v[86:87], v[32:33]
	v_mov_b32_e32 v91, v45
	v_mov_b32_e32 v62, v90
	v_pk_fma_f32 v[24:25], v[42:43], v[122:123], v[24:25]
	s_nop 0
	v_pk_fma_f32 v[24:25], v[90:91], v[62:63], v[24:25]
	s_nop 0
	v_fma_f32 v24, v25, v25, v24
	v_mov_b32_e32 v91, v25
	ds_bpermute_b32 v25, v188, v24
	s_waitcnt lgkmcnt(0)
	v_add_f32_e32 v24, v24, v25
	ds_bpermute_b32 v25, v189, v24
	s_waitcnt lgkmcnt(0)
	v_add_f32_e32 v24, v24, v25
	ds_bpermute_b32 v25, v190, v24
	s_waitcnt lgkmcnt(0)
	v_add_f32_e32 v24, v24, v25
	ds_bpermute_b32 v25, v191, v24
	s_waitcnt lgkmcnt(0)
	v_add_f32_e32 v24, v24, v25
	ds_bpermute_b32 v25, v192, v24
	s_waitcnt lgkmcnt(0)
	v_add_f32_e32 v24, v24, v25
	ds_bpermute_b32 v25, v193, v24
	s_waitcnt lgkmcnt(0)
	v_add_f32_e32 v24, v24, v25
	v_fmamk_f32 v24, v24, 0x3a800000, v16
	v_mul_f32_e32 v25, 0x4f800000, v24
	v_cmp_gt_f32_e32 vcc, s5, v24
	s_nop 1
	v_cndmask_b32_e32 v24, v24, v25, vcc
	v_sqrt_f32_e32 v25, v24
	s_nop 0
	v_add_u32_e32 v32, -1, v25
	v_add_u32_e32 v33, 1, v25
	v_fma_f32 v35, -v32, v25, v24
	v_fma_f32 v42, -v33, v25, v24
	v_cmp_ge_f32_e64 s[0:1], 0, v35
	s_nop 1
	v_cndmask_b32_e64 v25, v25, v32, s[0:1]
	v_cmp_lt_f32_e64 s[0:1], 0, v42
	s_nop 1
	v_cndmask_b32_e64 v25, v25, v33, s[0:1]
	v_mul_f32_e32 v32, 0x37800000, v25
	v_cndmask_b32_e32 v25, v25, v32, vcc
	v_cmp_class_f32_e32 vcc, v24, v34
	s_nop 1
	v_cndmask_b32_e32 v24, v25, v24, vcc
	v_div_scale_f32 v25, s[0:1], v24, v24, 1.0
	v_rcp_f32_e32 v33, v25
	v_div_scale_f32 v32, vcc, 1.0, v24, 1.0
	v_fma_f32 v35, -v25, v33, 1.0
	v_fmac_f32_e32 v33, v35, v33
	v_mul_f32_e32 v35, v32, v33
	v_fma_f32 v42, -v25, v35, v32
	v_fmac_f32_e32 v35, v42, v33
	v_fma_f32 v25, -v25, v35, v32
	v_div_fmas_f32 v25, v25, v33, v35
	v_div_fixup_f32 v24, v25, v24, 1.0
	v_pk_mul_f32 v[32:33], v[40:41], v[24:25] op_sel_hi:[1,0]
	v_pk_mul_f32 v[30:31], v[30:31], v[24:25] op_sel_hi:[1,0]
	v_pk_mul_f32 v[40:41], v[88:89], v[24:25] op_sel_hi:[1,0]
	v_pk_mul_f32 v[28:29], v[28:29], v[24:25] op_sel_hi:[1,0]
	v_pk_mul_f32 v[36:37], v[36:37], v[24:25] op_sel_hi:[1,0]
	v_pk_mul_f32 v[38:39], v[38:39], v[24:25] op_sel_hi:[1,0]
	v_pk_mul_f32 v[44:45], v[26:27], v[24:25] op_sel_hi:[1,0]
	v_pk_mul_f32 v[42:43], v[90:91], v[24:25] op_sel_hi:[1,0]
	v_pk_mul_f32 v[26:27], v[2:3], v[30:31]
	v_pk_mul_f32 v[24:25], v[0:1], v[32:33]
	v_pk_mul_f32 v[30:31], v[6:7], v[28:29]
	v_pk_mul_f32 v[28:29], v[4:5], v[40:41]
	v_pk_mul_f32 v[38:39], v[10:11], v[38:39]
	v_pk_mul_f32 v[36:37], v[8:9], v[36:37]
	v_pk_mul_f32 v[42:43], v[14:15], v[42:43]
	v_pk_mul_f32 v[40:41], v[12:13], v[44:45]
	global_store_dwordx4 v[22:23], v[24:27], off offset:-2048 sc1
	global_store_dwordx4 v[22:23], v[28:31], off offset:-1024 sc1
	global_store_dwordx4 v[22:23], v[36:39], off sc1
	global_store_dwordx4 v[22:23], v[40:43], off offset:1024 sc1
	v_lshl_add_u64 v[22:23], v[22:23], 0, s[8:9]
	s_cbranch_scc0 .LBB0_718
